# cb2_token_index_loads_issued_together
# baseline (speedup 1.0000x reference)
; __device__ __forceinline__ f32x4 ld_bf4(const bf16_t* p) { const u32x2 w = *(const u32x2*)p; return (f32x4){bf_lo(w.x), bf_hi(w.x), bf_lo(w.y), bf_hi(w.y)}; }
; template <int NTK>
; __device__ __forceinline__ void combine_rows(int t0, int tstride, const LAS int* bst, const int* tok_e, const int* tok_pos, const float* tok_w, const bf16_t* Y, const bf16_t* xbi, float* xio, bf16_t* xb, float* part, const float* gfin, bool last, int lane) {
;     ...
;     for (int i = 0; i < NTK; ++i) { const int t = t0 + i * tstride; ok[i] = t < T; tk[i] = ok[i] ? t : T - 1; }
; #pragma unroll
;     for (int i = 0; i < NTK; ++i) { const int t = tk[i]; const int e0 = tok_e[2 * t], e1 = tok_e[2 * t + 1]; w0[i] = tok_w[2 * t]; w1[i] = tok_w[2 * t + 1];
;         s0[i] = (size_t)bst[e0] * 256 + tok_pos[2 * t]; s1[i] = (size_t)bst[e1] * 256 + tok_pos[2 * t + 1]; }
;     f32x4 v[NTK][4]; u32x2 ya[NTK][4], yb[NTK][4];
; #pragma unroll
;     for (int i = 0; i < NTK; ++i)
; #pragma unroll
;         for (int j = 0; j < 4; ++j) { const int c = j * 256 + lane * 4; v[i][j] = ld_bf4(xbi + (size_t)tk[i] * DM + c); ya[i][j] = *(const u32x2*)(Y + s0[i] * DM + c); yb[i][j] = *(const u32x2*)(Y + s1[i] * DM + c); }
.LBB0_1633:
	s_add_i32 s6, s54, s12
	s_cmpk_lt_i32 s6, 0x4000
	s_cselect_b64 s[28:29], -1, 0
	s_and_b64 s[2:3], s[28:29], exec
	v_readlane_b32 s2, v252, 24
	s_cselect_b32 s26, s6, 0x3fff
	s_add_i32 s6, s2, s12
	s_cmpk_lt_i32 s6, 0x4000
	s_cselect_b64 s[24:25], -1, 0
	s_and_b64 s[2:3], s[24:25], exec
	v_readlane_b32 s2, v251, 2
	s_mul_i32 s2, s2, 24
	s_cselect_b32 s22, s6, 0x3fff
	s_add_i32 s6, s2, s12
	s_cmpk_lt_i32 s6, 0x4000
	s_cselect_b64 s[20:21], -1, 0
	s_and_b64 s[2:3], s[20:21], exec
	s_cselect_b32 s18, s6, 0x3fff
	s_ashr_i32 s17, s16, 31
	s_lshl_b64 s[6:7], s[16:17], 2
	v_readlane_b32 s10, v251, 34
	v_readlane_b32 s11, v251, 35
	s_add_u32 s2, s10, s6
	s_addc_u32 s3, s11, s7
	global_load_dwordx2 v[14:15], v161, s[2:3]
	s_add_i32 s2, s16, 1
	s_ashr_i32 s3, s2, 31
	v_readlane_b32 s34, v251, 38
	v_readlane_b32 s35, v251, 39
	s_add_u32 s8, s34, s6
	s_addc_u32 s9, s35, s7
	global_load_dword v82, v161, s[8:9]
	s_lshl_b64 s[8:9], s[2:3], 2
	s_add_u32 s2, s34, s8
	s_addc_u32 s3, s35, s9
	global_load_dword v84, v161, s[2:3]
	s_add_i32 s2, 0, 0x23900
	v_readlane_b32 s30, v251, 36
	v_readlane_b32 s31, v251, 37
	s_add_u32 s6, s30, s6
	s_addc_u32 s7, s31, s7
	global_load_dword v44, v161, s[6:7]
	s_add_u32 s6, s30, s8
	s_addc_u32 s7, s31, s9
	global_load_dword v46, v161, s[6:7]
	s_lshl_b32 s6, s26, 1
	s_ashr_i32 s7, s6, 31
	s_lshl_b64 s[6:7], s[6:7], 2
	s_add_u32 s8, s10, s6
	s_addc_u32 s9, s11, s7
	s_lshl_b32 s6, s26, 1
	s_ashr_i32 s7, s6, 31
	s_lshl_b64 s[6:7], s[6:7], 2
	s_add_u32 s8, s10, s6
	s_addc_u32 s9, s11, s7
	global_load_dwordx2 v[142:143], v161, s[8:9]
	s_add_u32 s8, s34, s6
	s_addc_u32 s9, s35, s7
	global_load_dwordx2 v[64:65], v161, s[8:9]
	s_add_u32 s8, s30, s6
	s_addc_u32 s9, s31, s7
	global_load_dwordx2 v[16:17], v161, s[8:9]
	s_lshl_b32 s6, s22, 1
	s_ashr_i32 s7, s6, 31
	s_lshl_b64 s[6:7], s[6:7], 2
	s_add_u32 s8, s10, s6
	s_addc_u32 s9, s11, s7
	global_load_dwordx2 v[144:145], v161, s[8:9]
	s_add_u32 s8, s34, s6
	s_addc_u32 s9, s35, s7
	global_load_dwordx2 v[146:147], v161, s[8:9]
	s_add_u32 s8, s30, s6
	s_addc_u32 s9, s31, s7
	global_load_dwordx2 v[18:19], v161, s[8:9]
	s_lshl_b32 s6, s18, 1
	s_ashr_i32 s7, s6, 31
	s_lshl_b64 s[6:7], s[6:7], 2
	s_add_u32 s8, s10, s6
	s_addc_u32 s9, s11, s7
	global_load_dwordx2 v[148:149], v161, s[8:9]
	s_add_u32 s8, s34, s6
	s_addc_u32 s9, s35, s7
	global_load_dwordx2 v[150:151], v161, s[8:9]
	s_add_u32 s8, s30, s6
	s_addc_u32 s9, s31, s7
	global_load_dwordx2 v[48:49], v161, s[8:9]
	v_lshl_add_u64 v[102:103], s[52:53], 0, v[8:9]
	s_waitcnt vmcnt(0)
	v_lshlrev_b32_e32 v14, 2, v14
	v_add_u32_e32 v14, s2, v14
	ds_read_b32 v38, v14
	v_lshlrev_b32_e32 v14, 2, v15
	v_add_u32_e32 v14, s2, v14
	ds_read_b32 v42, v14
	s_add_u32 s8, s34, s6
	s_addc_u32 s9, s35, s7
	s_add_u32 s6, s30, s6
	s_addc_u32 s7, s31, s7
	s_lshl_b32 s6, s22, 1
	s_ashr_i32 s7, s6, 31
	s_lshl_b64 s[6:7], s[6:7], 2
	s_add_u32 s8, s10, s6
	s_addc_u32 s9, s11, s7
	s_waitcnt lgkmcnt(1)
	v_ashrrev_i32_e32 v39, 31, v38
	v_ashrrev_i32_e32 v45, 31, v44
	s_waitcnt lgkmcnt(0)
	v_ashrrev_i32_e32 v43, 31, v42
	v_lshlrev_b64 v[38:39], 19, v[38:39]
	v_ashrrev_i32_e32 v47, 31, v46
	v_lshlrev_b64 v[44:45], 11, v[44:45]
	v_lshlrev_b64 v[42:43], 19, v[42:43]
	s_waitcnt vmcnt(2)
	v_lshlrev_b32_e32 v14, 2, v142
	v_add_u32_e32 v14, s2, v14
	ds_read_b32 v20, v14
	v_lshlrev_b32_e32 v14, 2, v143
	v_add_u32_e32 v14, s2, v14
	ds_read_b32 v26, v14
	s_add_u32 s8, s34, s6
	s_addc_u32 s9, s35, s7
	s_add_u32 s6, s30, s6
	s_addc_u32 s7, s31, s7
	s_waitcnt vmcnt(1)
	v_ashrrev_i32_e32 v25, 31, v16
	v_mov_b32_e32 v24, v16
	v_ashrrev_i32_e32 v29, 31, v17
	v_mov_b32_e32 v28, v17
	s_lshl_b32 s6, s18, 1
	s_ashr_i32 s7, s6, 31
	s_lshl_b64 s[6:7], s[6:7], 2
	s_add_u32 s8, s10, s6
	s_addc_u32 s9, s11, s7
	s_waitcnt lgkmcnt(1)
	v_ashrrev_i32_e32 v21, 31, v20
	v_lshlrev_b64 v[20:21], 19, v[20:21]
	s_waitcnt lgkmcnt(0)
	v_ashrrev_i32_e32 v27, 31, v26
	v_lshlrev_b64 v[24:25], 11, v[24:25]
	s_waitcnt vmcnt(2)
	v_lshlrev_b32_e32 v14, 2, v144
	v_add_u32_e32 v14, s2, v14
	ds_read_b32 v30, v14
	s_waitcnt vmcnt(0)
	v_ashrrev_i32_e32 v33, 31, v18
	v_mov_b32_e32 v32, v18
	v_ashrrev_i32_e32 v37, 31, v19
	v_mov_b32_e32 v36, v19
	s_add_u32 s8, s34, s6
	s_addc_u32 s9, s35, s7
	s_add_u32 s6, s30, s6
	s_addc_u32 s7, s31, s7
	s_ashr_i32 s27, s26, 31
	s_ashr_i32 s23, s22, 31
	s_ashr_i32 s19, s18, 31
	s_waitcnt vmcnt(1)
	v_lshlrev_b32_e32 v18, 2, v148
	v_add_u32_e32 v18, s2, v18
	ds_read_b32 v40, v18
	v_lshlrev_b32_e32 v14, 2, v145
	v_lshlrev_b32_e32 v18, 2, v149
	v_add_u32_e32 v14, s2, v14
	v_add_u32_e32 v18, s2, v18
	ds_read_b32 v34, v14
	ds_read_b32 v18, v18
	v_readlane_b32 s8, v251, 56
	v_readlane_b32 s9, v251, 57
	s_mov_b32 s2, 0x2a00000
	s_waitcnt lgkmcnt(3)
	v_ashrrev_i32_e32 v31, 31, v30
	v_lshl_add_u64 v[38:39], s[8:9], 0, v[38:39]
	v_lshl_add_u64 v[38:39], v[38:39], 0, v[44:45]
	v_lshlrev_b64 v[44:45], 11, v[46:47]
	v_lshl_add_u64 v[42:43], s[8:9], 0, v[42:43]
	v_lshl_add_u64 v[42:43], v[42:43], 0, v[44:45]
	v_add_co_u32_e32 v44, vcc, s2, v102
	v_readfirstlane_b32 s6, v38
	s_nop 0
	v_addc_co_u32_e32 v45, vcc, 0, v103, vcc
	v_readfirstlane_b32 s7, v39
	v_readfirstlane_b32 s10, v42
	v_readfirstlane_b32 s11, v43
	global_load_dwordx2 v[46:47], v[44:45], off
	v_lshl_add_u64 v[20:21], s[8:9], 0, v[20:21]
	v_lshl_add_u64 v[20:21], v[20:21], 0, v[24:25]
	global_load_dwordx2 v[110:111], v140, s[6:7]
	s_nop 0
	global_load_dwordx2 v[108:109], v140, s[10:11]
	global_load_dwordx2 v[38:39], v[44:45], off offset:512
	v_lshlrev_b64 v[24:25], 19, v[26:27]
	s_lshl_b64 s[2:3], s[26:27], 11
	v_lshlrev_b64 v[26:27], 11, v[28:29]
	v_lshl_add_u64 v[24:25], s[8:9], 0, v[24:25]
	v_lshl_add_u64 v[24:25], v[24:25], 0, v[26:27]
	v_lshl_add_u64 v[72:73], v[4:5], 0, s[2:3]
	v_readfirstlane_b32 s2, v20
	v_readfirstlane_b32 s3, v21
	v_lshlrev_b64 v[20:21], 19, v[30:31]
	s_waitcnt lgkmcnt(1)
; __device__ __forceinline__ float bf_lo(unsigned w) { return __uint_as_float(w << 16); }
; __device__ __forceinline__ float bf_hi(unsigned w) { return __uint_as_float(w & 0xffff0000u); }
; __device__ __forceinline__ f32x4 ld_bf4(const bf16_t* p) { const u32x2 w = *(const u32x2*)p; return (f32x4){bf_lo(w.x), bf_hi(w.x), bf_lo(w.y), bf_hi(w.y)}; }
; template <int NTK>
; __device__ __forceinline__ void combine_rows(int t0, int tstride, const LAS int* bst, const int* tok_e, const int* tok_pos, const float* tok_w, const bf16_t* Y, const bf16_t* xbi, float* xio, bf16_t* xb, float* part, const float* gfin, bool last, int lane) {
;     ...
;     for (int i = 0; i < NTK; ++i) { const int t = tk[i]; const int e0 = tok_e[2 * t], e1 = tok_e[2 * t + 1]; w0[i] = tok_w[2 * t]; w1[i] = tok_w[2 * t + 1];
;         s0[i] = (size_t)bst[e0] * 256 + tok_pos[2 * t]; s1[i] = (size_t)bst[e1] * 256 + tok_pos[2 * t + 1]; }
;     f32x4 v[NTK][4]; u32x2 ya[NTK][4], yb[NTK][4];
; #pragma unroll
;     for (int i = 0; i < NTK; ++i)
; #pragma unroll
;         for (int j = 0; j < 4; ++j) { const int c = j * 256 + lane * 4; v[i][j] = ld_bf4(xbi + (size_t)tk[i] * DM + c); ya[i][j] = *(const u32x2*)(Y + s0[i] * DM + c); yb[i][j] = *(const u32x2*)(Y + s1[i] * DM + c); }
; #pragma unroll
;     for (int i = 0; i < NTK; ++i) { float s = 0.f;
; #pragma unroll
;         for (int j = 0; j < 4; ++j) { const f32x4 a = {bf_lo(ya[i][j].x), bf_hi(ya[i][j].x), bf_lo(ya[i][j].y), bf_hi(ya[i][j].y)}, b = {bf_lo(yb[i][j].x), bf_hi(yb[i][j].x), bf_lo(yb[i][j].y), bf_hi(yb[i][j].y)};
;             v[i][j] = v[i][j] + w0[i] * a + w1[i] * b;
;             s += (v[i][j][0] * v[i][j][0] + v[i][j][1] * v[i][j][1]) + (v[i][j][2] * v[i][j][2] + v[i][j][3] * v[i][j][3]); }
	v_ashrrev_i32_e32 v35, 31, v34
	v_lshl_add_u64 v[20:21], s[8:9], 0, v[20:21]
	v_ashrrev_i32_e32 v41, 31, v40
	s_waitcnt lgkmcnt(0)
	v_ashrrev_i32_e32 v19, 31, v18
	v_lshlrev_b64 v[26:27], 11, v[36:37]
	v_lshlrev_b64 v[18:19], 19, v[18:19]
	v_lshl_add_u64 v[18:19], s[8:9], 0, v[18:19]
	s_andn2_b64 vcc, exec, s[14:15]
	s_waitcnt vmcnt(5)
	v_ashrrev_i32_e32 v67, 31, v48
	v_mov_b32_e32 v66, v48
	v_ashrrev_i32_e32 v23, 31, v49
	v_mov_b32_e32 v22, v49
	v_lshlrev_b64 v[22:23], 11, v[22:23]
	v_lshl_add_u64 v[22:23], v[18:19], 0, v[22:23]
	s_waitcnt vmcnt(3)
	v_lshlrev_b32_e32 v106, 16, v46
	v_and_b32_e32 v107, 0xffff0000, v46
	v_lshlrev_b32_e32 v104, 16, v47
	v_and_b32_e32 v105, 0xffff0000, v47
	s_waitcnt vmcnt(0)
	v_lshlrev_b32_e32 v118, 16, v38
	v_and_b32_e32 v119, 0xffff0000, v38
	v_lshlrev_b32_e32 v114, 16, v39
	v_and_b32_e32 v115, 0xffff0000, v39
	global_load_dwordx2 v[130:131], v140, s[6:7] offset:512
	global_load_dwordx2 v[126:127], v140, s[10:11] offset:512
	global_load_dwordx2 v[38:39], v[44:45], off offset:1024
	v_lshlrev_b32_e32 v136, 16, v110
	v_and_b32_e32 v137, 0xffff0000, v110
	v_lshlrev_b32_e32 v110, 16, v111
	v_and_b32_e32 v111, 0xffff0000, v111
	v_lshlrev_b32_e32 v138, 16, v108
	v_and_b32_e32 v139, 0xffff0000, v108
	v_lshlrev_b32_e32 v108, 16, v109
	v_and_b32_e32 v109, 0xffff0000, v109
	v_pk_fma_f32 v[106:107], v[82:83], v[136:137], v[106:107] op_sel_hi:[0,1,1]
	v_pk_fma_f32 v[104:105], v[82:83], v[110:111], v[104:105] op_sel_hi:[0,1,1]
	v_pk_fma_f32 v[136:137], v[84:85], v[108:109], v[104:105] op_sel_hi:[0,1,1]
	v_pk_fma_f32 v[138:139], v[84:85], v[138:139], v[106:107] op_sel_hi:[0,1,1]
	v_mul_f32_e32 v83, v139, v139
	v_mul_f32_e32 v85, v137, v137
	v_fmac_f32_e32 v83, v138, v138
	v_fmac_f32_e32 v85, v136, v136
	v_add_f32_e32 v83, v83, v85
	s_waitcnt vmcnt(2)
	v_lshlrev_b32_e32 v104, 16, v130
	v_and_b32_e32 v105, 0xffff0000, v130
	s_waitcnt vmcnt(0)
	v_lshlrev_b32_e32 v116, 16, v38
	v_and_b32_e32 v117, 0xffff0000, v38
	v_lshlrev_b32_e32 v112, 16, v39
	v_and_b32_e32 v113, 0xffff0000, v39
	global_load_dwordx2 v[128:129], v140, s[6:7] offset:1024
	global_load_dwordx2 v[124:125], v140, s[10:11] offset:1024
	global_load_dwordx2 v[38:39], v[44:45], off offset:1536
	global_load_dwordx2 v[134:135], v140, s[6:7] offset:1536
	global_load_dwordx2 v[132:133], v140, s[10:11] offset:1536
	v_readfirstlane_b32 s6, v24
	v_readfirstlane_b32 s7, v25
	v_lshlrev_b64 v[24:25], 11, v[32:33]
	v_lshl_add_u64 v[24:25], v[20:21], 0, v[24:25]
	v_lshlrev_b64 v[20:21], 19, v[34:35]
	global_load_dwordx2 v[94:95], v[72:73], off
	global_load_dwordx2 v[92:93], v140, s[2:3]
	global_load_dwordx2 v[90:91], v140, s[6:7]
	global_load_dwordx2 v[100:101], v[72:73], off offset:512
	global_load_dwordx2 v[88:89], v140, s[2:3] offset:512
	global_load_dwordx2 v[86:87], v140, s[6:7] offset:512
	global_load_dwordx2 v[98:99], v[72:73], off offset:1024
	global_load_dwordx2 v[80:81], v140, s[2:3] offset:1024
	global_load_dwordx2 v[78:79], v140, s[6:7] offset:1024
	global_load_dwordx2 v[96:97], v[72:73], off offset:1536
	global_load_dwordx2 v[76:77], v140, s[2:3] offset:1536
	global_load_dwordx2 v[74:75], v140, s[6:7] offset:1536
	s_lshl_b64 s[2:3], s[22:23], 11
	v_lshl_add_u64 v[20:21], s[8:9], 0, v[20:21]
	v_lshl_add_u64 v[26:27], v[20:21], 0, v[26:27]
	v_lshl_add_u64 v[20:21], v[4:5], 0, s[2:3]
	v_readfirstlane_b32 s2, v24
	v_readfirstlane_b32 s3, v25
	v_lshlrev_b64 v[24:25], 19, v[40:41]
	v_readfirstlane_b32 s6, v26
	v_readfirstlane_b32 s7, v27
	v_lshlrev_b64 v[26:27], 11, v[66:67]
	v_lshl_add_u64 v[24:25], s[8:9], 0, v[24:25]
	global_load_dwordx2 v[56:57], v[20:21], off
	global_load_dwordx2 v[54:55], v140, s[2:3]
	v_lshl_add_u64 v[24:25], v[24:25], 0, v[26:27]
	v_readfirstlane_b32 s10, v22
	v_readfirstlane_b32 s11, v23
	v_lshlrev_b32_e32 v106, 16, v131
	v_and_b32_e32 v107, 0xffff0000, v131
	v_lshlrev_b32_e32 v108, 16, v126
	v_and_b32_e32 v109, 0xffff0000, v126
	v_lshlrev_b32_e32 v110, 16, v127
	v_and_b32_e32 v111, 0xffff0000, v127
	v_pk_fma_f32 v[118:119], v[82:83], v[104:105], v[118:119] op_sel_hi:[0,1,1]
	v_pk_fma_f32 v[104:105], v[82:83], v[106:107], v[114:115] op_sel_hi:[0,1,1]
	v_pk_fma_f32 v[104:105], v[84:85], v[110:111], v[104:105] op_sel_hi:[0,1,1]
	v_pk_fma_f32 v[108:109], v[84:85], v[108:109], v[118:119] op_sel_hi:[0,1,1]
	v_mul_f32_e32 v85, v109, v109
	v_mul_f32_e32 v106, v105, v105
	v_fmac_f32_e32 v85, v108, v108
	v_fmac_f32_e32 v106, v104, v104
	v_add_f32_e32 v85, v85, v106
	v_add_f32_e32 v83, v83, v85
	s_waitcnt vmcnt(18)
	v_lshlrev_b32_e32 v106, 16, v128
	v_and_b32_e32 v107, 0xffff0000, v128
	s_waitcnt vmcnt(16)
; __device__ __forceinline__ float bf_lo(unsigned w) { return __uint_as_float(w << 16); }
; __device__ __forceinline__ float bf_hi(unsigned w) { return __uint_as_float(w & 0xffff0000u); }
; __device__ __forceinline__ float wave_sum(float v) { return half_sum(sum32(v)); }
; __device__ __forceinline__ f32x4 ld_bf4(const bf16_t* p) { const u32x2 w = *(const u32x2*)p; return (f32x4){bf_lo(w.x), bf_hi(w.x), bf_lo(w.y), bf_hi(w.y)}; }
; __device__ __forceinline__ void st_bf4(bf16_t* p, f32x4 v) { u32x2 w; w.x = cvt_pk_bf16(v[0], v[1]); w.y = cvt_pk_bf16(v[2], v[3]); *(u32x2*)p = w; }
; template <int NTK>
; __device__ __forceinline__ void combine_rows(int t0, int tstride, const LAS int* bst, const int* tok_e, const int* tok_pos, const float* tok_w, const bf16_t* Y, const bf16_t* xbi, float* xio, bf16_t* xb, float* part, const float* gfin, bool last, int lane) {
;     ...
;         for (int j = 0; j < 4; ++j) { const int c = j * 256 + lane * 4; v[i][j] = ld_bf4(xbi + (size_t)tk[i] * DM + c); ya[i][j] = *(const u32x2*)(Y + s0[i] * DM + c); yb[i][j] = *(const u32x2*)(Y + s1[i] * DM + c); }
; #pragma unroll
;     for (int i = 0; i < NTK; ++i) { float s = 0.f;
; #pragma unroll
;         for (int j = 0; j < 4; ++j) { const f32x4 a = {bf_lo(ya[i][j].x), bf_hi(ya[i][j].x), bf_lo(ya[i][j].y), bf_hi(ya[i][j].y)}, b = {bf_lo(yb[i][j].x), bf_hi(yb[i][j].x), bf_lo(yb[i][j].y), bf_hi(yb[i][j].y)};
;             v[i][j] = v[i][j] + w0[i] * a + w1[i] * b;
;             s += (v[i][j][0] * v[i][j][0] + v[i][j][1] * v[i][j][1]) + (v[i][j][2] * v[i][j][2] + v[i][j][3] * v[i][j][3]); }
;         s = wave_sum(s);
;         if (ok[i]) { const int t = tk[i];
;             if (!last) {
; #pragma unroll
;                 for (int j = 0; j < 4; ++j) { const int c = j * 256 + lane * 4; st_bf4(xb + (size_t)t * DM + c, v[i][j]); }
;                 if (lane < 16) part[(size_t)t * 16 + lane] = lane == 0 ? s : 0.f;
	v_lshlrev_b32_e32 v122, 16, v38
	v_and_b32_e32 v123, 0xffff0000, v38
	v_lshlrev_b32_e32 v120, 16, v39
	v_and_b32_e32 v121, 0xffff0000, v39
	global_load_dwordx2 v[52:53], v140, s[6:7]
	global_load_dwordx2 v[62:63], v[20:21], off offset:512
	global_load_dwordx2 v[50:51], v140, s[2:3] offset:512
	global_load_dwordx2 v[48:49], v140, s[6:7] offset:512
	global_load_dwordx2 v[60:61], v[20:21], off offset:1024
	global_load_dwordx2 v[46:47], v140, s[2:3] offset:1024
	global_load_dwordx2 v[44:45], v140, s[6:7] offset:1024
	global_load_dwordx2 v[58:59], v[20:21], off offset:1536
	global_load_dwordx2 v[38:39], v140, s[2:3] offset:1536
	global_load_dwordx2 v[36:37], v140, s[6:7] offset:1536
	s_lshl_b64 s[6:7], s[18:19], 11
	v_lshl_add_u64 v[18:19], v[4:5], 0, s[6:7]
	v_readfirstlane_b32 s6, v24
	v_readfirstlane_b32 s7, v25
	global_load_dwordx2 v[32:33], v[18:19], off
	v_lshlrev_b32_e32 v110, 16, v129
	v_and_b32_e32 v111, 0xffff0000, v129
	v_lshlrev_b32_e32 v114, 16, v124
	v_and_b32_e32 v115, 0xffff0000, v124
	global_load_dwordx2 v[30:31], v140, s[6:7]
	global_load_dwordx2 v[34:35], v140, s[10:11]
	global_load_dwordx2 v[40:41], v[18:19], off offset:512
	global_load_dwordx2 v[26:27], v140, s[6:7] offset:512
	global_load_dwordx2 v[28:29], v140, s[10:11] offset:512
	global_load_dwordx2 v[42:43], v[18:19], off offset:1024
	global_load_dwordx2 v[22:23], v140, s[6:7] offset:1024
	global_load_dwordx2 v[24:25], v140, s[10:11] offset:1024
	global_load_dwordx2 v[70:71], v[18:19], off offset:1536
	global_load_dwordx2 v[66:67], v140, s[6:7] offset:1536
	global_load_dwordx2 v[68:69], v140, s[10:11] offset:1536
	v_lshlrev_b32_e32 v118, 16, v125
	v_and_b32_e32 v119, 0xffff0000, v125
	v_pk_fma_f32 v[116:117], v[82:83], v[106:107], v[116:117] op_sel_hi:[0,1,1]
	v_pk_fma_f32 v[106:107], v[82:83], v[110:111], v[112:113] op_sel_hi:[0,1,1]
	v_pk_fma_f32 v[106:107], v[84:85], v[118:119], v[106:107] op_sel_hi:[0,1,1]
	v_pk_fma_f32 v[110:111], v[84:85], v[114:115], v[116:117] op_sel_hi:[0,1,1]
	v_mul_f32_e32 v85, v111, v111
	v_mul_f32_e32 v112, v107, v107
	v_fmac_f32_e32 v85, v110, v110
	v_fmac_f32_e32 v112, v106, v106
	v_add_f32_e32 v85, v85, v112
	s_waitcnt vmcnt(37)
	v_lshlrev_b32_e32 v112, 16, v134
	v_and_b32_e32 v113, 0xffff0000, v134
	v_lshlrev_b32_e32 v114, 16, v135
	v_and_b32_e32 v115, 0xffff0000, v135
	v_add_f32_e32 v124, v83, v85
	s_waitcnt vmcnt(36)
	v_lshlrev_b32_e32 v116, 16, v132
	v_and_b32_e32 v117, 0xffff0000, v132
	v_lshlrev_b32_e32 v118, 16, v133
	v_and_b32_e32 v119, 0xffff0000, v133
	v_pk_fma_f32 v[112:113], v[82:83], v[112:113], v[122:123] op_sel_hi:[0,1,1]
	v_pk_fma_f32 v[82:83], v[82:83], v[114:115], v[120:121] op_sel_hi:[0,1,1]
	v_pk_fma_f32 v[82:83], v[84:85], v[118:119], v[82:83] op_sel_hi:[0,1,1]
	v_pk_fma_f32 v[84:85], v[84:85], v[116:117], v[112:113] op_sel_hi:[0,1,1]
	v_mul_f32_e32 v112, v85, v85
	v_mul_f32_e32 v113, v83, v83
	v_fmac_f32_e32 v112, v84, v84
	v_fmac_f32_e32 v113, v82, v82
	v_add_f32_e32 v112, v112, v113
	v_add_f32_e32 v112, v124, v112
	ds_swizzle_b32 v113, v112 offset:swizzle(SWAP,1)
	s_mov_b64 s[10:11], -1
	s_waitcnt lgkmcnt(0)
	v_add_f32_e32 v112, v112, v113
	ds_swizzle_b32 v113, v112 offset:swizzle(SWAP,2)
	s_waitcnt lgkmcnt(0)
	v_add_f32_e32 v112, v112, v113
	ds_swizzle_b32 v113, v112 offset:swizzle(SWAP,4)
	s_waitcnt lgkmcnt(0)
	v_add_f32_e32 v112, v112, v113
	ds_swizzle_b32 v113, v112 offset:swizzle(SWAP,8)
	s_waitcnt lgkmcnt(0)
	v_add_f32_e32 v112, v112, v113
	ds_swizzle_b32 v113, v112 offset:swizzle(SWAP,16)
	s_waitcnt lgkmcnt(0)
	v_add_f32_e32 v112, v112, v113
	v_mov_b32_e32 v113, v112
	s_nop 1
	v_permlane32_swap_b32_e32 v112, v113
	v_add_f32_e32 v112, v112, v113
	v_cndmask_b32_e64 v113, 0, 1, s[14:15]
	v_cmp_ne_u32_e64 s[6:7], 1, v113
	s_cbranch_vccnz .LBB0_1637
	s_mov_b64 s[2:3], 0x2a00000
	v_lshl_add_u64 v[114:115], v[102:103], 0, s[2:3]
	s_mov_b64 s[2:3], 0x2a00200
	v_lshl_add_u64 v[116:117], v[102:103], 0, s[2:3]
	s_mov_b64 s[2:3], 0x2a00400
	v_lshl_add_u64 v[118:119], v[102:103], 0, s[2:3]
	s_mov_b64 s[2:3], 0x2a00600
	v_cvt_pk_bf16_f32 v120, v138, v139
	v_cvt_pk_bf16_f32 v121, v136, v137
	global_store_dwordx2 v[114:115], v[120:121], off
	v_cvt_pk_bf16_f32 v114, v108, v109
	v_cvt_pk_bf16_f32 v115, v104, v105
	v_lshl_add_u64 v[102:103], v[102:103], 0, s[2:3]
	global_store_dwordx2 v[116:117], v[114:115], off
	v_cvt_pk_bf16_f32 v114, v110, v111
	v_cvt_pk_bf16_f32 v115, v106, v107
	global_store_dwordx2 v[118:119], v[114:115], off
	v_cvt_pk_bf16_f32 v114, v84, v85
	v_cvt_pk_bf16_f32 v115, v82, v83
	global_store_dwordx2 v[102:103], v[114:115], off
	s_and_saveexec_b64 s[10:11], s[0:1]
	s_cbranch_execz .LBB0_1636
	v_cndmask_b32_e64 v113, 0, v112, s[4:5]
	v_lshl_add_u64 v[102:103], s[52:53], 0, v[12:13]
	global_store_dword v[102:103], v113, off

; __device__ __forceinline__ float bf_lo(unsigned w) { return __uint_as_float(w << 16); }
; __device__ __forceinline__ float bf_hi(unsigned w) { return __uint_as_float(w & 0xffff0000u); }
; __device__ __forceinline__ float wave_sum(float v) { return half_sum(sum32(v)); }
; __device__ __forceinline__ void st_bf4(bf16_t* p, f32x4 v) { u32x2 w; w.x = cvt_pk_bf16(v[0], v[1]); w.y = cvt_pk_bf16(v[2], v[3]); *(u32x2*)p = w; }
; template <int NTK>
; __device__ __forceinline__ void combine_rows(int t0, int tstride, const LAS int* bst, const int* tok_e, const int* tok_pos, const float* tok_w, const bf16_t* Y, const bf16_t* xbi, float* xio, bf16_t* xb, float* part, const float* gfin, bool last, int lane) {
;     ...
;         for (int j = 0; j < 4; ++j) { const f32x4 a = {bf_lo(ya[i][j].x), bf_hi(ya[i][j].x), bf_lo(ya[i][j].y), bf_hi(ya[i][j].y)}, b = {bf_lo(yb[i][j].x), bf_hi(yb[i][j].x), bf_lo(yb[i][j].y), bf_hi(yb[i][j].y)};
;             v[i][j] = v[i][j] + w0[i] * a + w1[i] * b;
;             s += (v[i][j][0] * v[i][j][0] + v[i][j][1] * v[i][j][1]) + (v[i][j][2] * v[i][j][2] + v[i][j][3] * v[i][j][3]); }
;         s = wave_sum(s);
;         if (ok[i]) { const int t = tk[i];
;             if (!last) {
; #pragma unroll
;                 for (int j = 0; j < 4; ++j) { const int c = j * 256 + lane * 4; st_bf4(xb + (size_t)t * DM + c, v[i][j]); }
;                 if (lane < 16) part[(size_t)t * 16 + lane] = lane == 0 ? s : 0.f;
.LBB0_1646:
	s_waitcnt vmcnt(23)
	v_lshlrev_b32_e32 v64, 16, v56
	v_and_b32_e32 v65, 0xffff0000, v56
	v_lshlrev_b32_e32 v56, 16, v57
	v_and_b32_e32 v57, 0xffff0000, v57
	s_waitcnt vmcnt(22)
	v_lshlrev_b32_e32 v78, 16, v54
	v_and_b32_e32 v79, 0xffff0000, v54
	v_lshlrev_b32_e32 v54, 16, v55
	v_and_b32_e32 v55, 0xffff0000, v55
	s_waitcnt vmcnt(21)
	v_lshlrev_b32_e32 v80, 16, v52
	v_and_b32_e32 v81, 0xffff0000, v52
	v_lshlrev_b32_e32 v52, 16, v53
	v_and_b32_e32 v53, 0xffff0000, v53
	v_pk_fma_f32 v[64:65], v[146:147], v[78:79], v[64:65] op_sel_hi:[0,1,1]
	v_pk_fma_f32 v[54:55], v[146:147], v[54:55], v[56:57] op_sel_hi:[0,1,1]
	v_pk_fma_f32 v[52:53], v[146:147], v[52:53], v[54:55] op_sel:[1,0,0]
	v_pk_fma_f32 v[54:55], v[146:147], v[80:81], v[64:65] op_sel:[1,0,0]
	v_mul_f32_e32 v57, v53, v53
	v_mul_f32_e32 v56, v55, v55
	v_fmac_f32_e32 v56, v54, v54
	v_fmac_f32_e32 v57, v52, v52
	s_waitcnt vmcnt(20)
	v_lshlrev_b32_e32 v72, 16, v62
	v_and_b32_e32 v73, 0xffff0000, v62
	v_lshlrev_b32_e32 v62, 16, v63
	v_and_b32_e32 v63, 0xffff0000, v63
	v_add_f32_e32 v78, v56, v57
	s_waitcnt vmcnt(19)
	v_lshlrev_b32_e32 v56, 16, v50
	v_and_b32_e32 v57, 0xffff0000, v50
	v_lshlrev_b32_e32 v50, 16, v51
	v_and_b32_e32 v51, 0xffff0000, v51
	s_waitcnt vmcnt(18)
	v_lshlrev_b32_e32 v64, 16, v48
	v_and_b32_e32 v65, 0xffff0000, v48
	v_lshlrev_b32_e32 v48, 16, v49
	v_and_b32_e32 v49, 0xffff0000, v49
	v_pk_fma_f32 v[56:57], v[146:147], v[56:57], v[72:73] op_sel_hi:[0,1,1]
	v_pk_fma_f32 v[50:51], v[146:147], v[50:51], v[62:63] op_sel_hi:[0,1,1]
	v_pk_fma_f32 v[48:49], v[146:147], v[48:49], v[50:51] op_sel:[1,0,0]
	v_pk_fma_f32 v[50:51], v[146:147], v[64:65], v[56:57] op_sel:[1,0,0]
	v_mul_f32_e32 v57, v49, v49
	v_mul_f32_e32 v56, v51, v51
	v_fmac_f32_e32 v56, v50, v50
	v_fmac_f32_e32 v57, v48, v48
	v_add_f32_e32 v56, v56, v57
	s_waitcnt vmcnt(17)
	v_lshlrev_b32_e32 v74, 16, v60
	v_and_b32_e32 v75, 0xffff0000, v60
	v_lshlrev_b32_e32 v60, 16, v61
	v_and_b32_e32 v61, 0xffff0000, v61
	v_add_f32_e32 v64, v78, v56
	s_waitcnt vmcnt(16)
	v_lshlrev_b32_e32 v56, 16, v46
	v_and_b32_e32 v57, 0xffff0000, v46
	v_lshlrev_b32_e32 v46, 16, v47
	v_and_b32_e32 v47, 0xffff0000, v47
	s_waitcnt vmcnt(15)
	v_lshlrev_b32_e32 v62, 16, v44
	v_and_b32_e32 v63, 0xffff0000, v44
	v_lshlrev_b32_e32 v44, 16, v45
	v_and_b32_e32 v45, 0xffff0000, v45
	v_pk_fma_f32 v[56:57], v[146:147], v[56:57], v[74:75] op_sel_hi:[0,1,1]
	v_pk_fma_f32 v[46:47], v[146:147], v[46:47], v[60:61] op_sel_hi:[0,1,1]
	v_pk_fma_f32 v[44:45], v[146:147], v[44:45], v[46:47] op_sel:[1,0,0]
	v_pk_fma_f32 v[46:47], v[146:147], v[62:63], v[56:57] op_sel:[1,0,0]
	v_mul_f32_e32 v57, v45, v45
	v_mul_f32_e32 v56, v47, v47
	v_fmac_f32_e32 v56, v46, v46
	v_fmac_f32_e32 v57, v44, v44
	v_add_f32_e32 v56, v56, v57
	s_waitcnt vmcnt(14)
	v_lshlrev_b32_e32 v76, 16, v58
	v_and_b32_e32 v77, 0xffff0000, v58
	v_lshlrev_b32_e32 v58, 16, v59
	v_and_b32_e32 v59, 0xffff0000, v59
	v_add_f32_e32 v62, v64, v56
	s_waitcnt vmcnt(13)
	v_lshlrev_b32_e32 v56, 16, v38
	v_and_b32_e32 v57, 0xffff0000, v38
	v_lshlrev_b32_e32 v38, 16, v39
	v_and_b32_e32 v39, 0xffff0000, v39
	s_waitcnt vmcnt(12)
	v_lshlrev_b32_e32 v60, 16, v36
	v_and_b32_e32 v61, 0xffff0000, v36
	v_lshlrev_b32_e32 v36, 16, v37
	v_and_b32_e32 v37, 0xffff0000, v37
	v_pk_fma_f32 v[56:57], v[146:147], v[56:57], v[76:77] op_sel_hi:[0,1,1]
	v_pk_fma_f32 v[38:39], v[146:147], v[38:39], v[58:59] op_sel_hi:[0,1,1]
	v_pk_fma_f32 v[36:37], v[146:147], v[36:37], v[38:39] op_sel:[1,0,0]
	v_pk_fma_f32 v[16:17], v[146:147], v[60:61], v[56:57] op_sel:[1,0,0]
	v_mul_f32_e32 v39, v37, v37
	v_mul_f32_e32 v38, v17, v17
	v_fmac_f32_e32 v38, v16, v16
	v_fmac_f32_e32 v39, v36, v36
	v_add_f32_e32 v38, v38, v39
	v_add_f32_e32 v38, v62, v38
	ds_swizzle_b32 v39, v38 offset:swizzle(SWAP,1)
	s_andn2_b64 vcc, exec, s[24:25]
	s_waitcnt lgkmcnt(0)
	v_add_f32_e32 v38, v38, v39
	ds_swizzle_b32 v39, v38 offset:swizzle(SWAP,2)
	s_waitcnt lgkmcnt(0)
	v_add_f32_e32 v38, v38, v39
	ds_swizzle_b32 v39, v38 offset:swizzle(SWAP,4)
	s_waitcnt lgkmcnt(0)
	v_add_f32_e32 v38, v38, v39
	ds_swizzle_b32 v39, v38 offset:swizzle(SWAP,8)
	s_waitcnt lgkmcnt(0)
	v_add_f32_e32 v38, v38, v39
	ds_swizzle_b32 v39, v38 offset:swizzle(SWAP,16)
	s_waitcnt lgkmcnt(0)
	v_add_f32_e32 v38, v38, v39
	v_mov_b32_e32 v39, v38
	s_nop 1
	v_permlane32_swap_b32_e32 v38, v39
	s_cbranch_vccnz .LBB0_1653
	v_add_f32_e32 v38, v38, v39
	s_and_b64 vcc, exec, s[6:7]
	s_mov_b64 s[10:11], -1
	s_cbranch_vccnz .LBB0_1651
	v_cvt_pk_bf16_f32 v56, v54, v55
	v_cvt_pk_bf16_f32 v57, v52, v53
	global_store_dwordx2 v[20:21], v[56:57], off
	v_cvt_pk_bf16_f32 v56, v50, v51
	v_cvt_pk_bf16_f32 v57, v48, v49
	global_store_dwordx2 v[20:21], v[56:57], off offset:512
	v_cvt_pk_bf16_f32 v56, v46, v47
	v_cvt_pk_bf16_f32 v57, v44, v45
	global_store_dwordx2 v[20:21], v[56:57], off offset:1024
	v_cvt_pk_bf16_f32 v56, v16, v17
	v_cvt_pk_bf16_f32 v57, v36, v37
	global_store_dwordx2 v[20:21], v[56:57], off offset:1536
	s_and_saveexec_b64 s[10:11], s[0:1]
	s_cbranch_execz .LBB0_1650
	s_lshl_b64 s[2:3], s[22:23], 6
	v_cndmask_b32_e64 v39, 0, v38, s[4:5]
	v_lshl_add_u64 v[20:21], v[0:1], 0, s[2:3]
	global_store_dword v[20:21], v39, off

; __device__ __forceinline__ float bf_lo(unsigned w) { return __uint_as_float(w << 16); }
; __device__ __forceinline__ float bf_hi(unsigned w) { return __uint_as_float(w & 0xffff0000u); }
; __device__ __forceinline__ float wave_sum(float v) { return half_sum(sum32(v)); }
; __device__ __forceinline__ void st_bf4(bf16_t* p, f32x4 v) { u32x2 w; w.x = cvt_pk_bf16(v[0], v[1]); w.y = cvt_pk_bf16(v[2], v[3]); *(u32x2*)p = w; }
; template <int NTK>
; __device__ __forceinline__ void combine_rows(int t0, int tstride, const LAS int* bst, const int* tok_e, const int* tok_pos, const float* tok_w, const bf16_t* Y, const bf16_t* xbi, float* xio, bf16_t* xb, float* part, const float* gfin, bool last, int lane) {
;     ...
;         for (int j = 0; j < 4; ++j) { const f32x4 a = {bf_lo(ya[i][j].x), bf_hi(ya[i][j].x), bf_lo(ya[i][j].y), bf_hi(ya[i][j].y)}, b = {bf_lo(yb[i][j].x), bf_hi(yb[i][j].x), bf_lo(yb[i][j].y), bf_hi(yb[i][j].y)};
;             v[i][j] = v[i][j] + w0[i] * a + w1[i] * b;
;             s += (v[i][j][0] * v[i][j][0] + v[i][j][1] * v[i][j][1]) + (v[i][j][2] * v[i][j][2] + v[i][j][3] * v[i][j][3]); }
;         s = wave_sum(s);
;         if (ok[i]) { const int t = tk[i];
;             if (!last) {
; #pragma unroll
;                 for (int j = 0; j < 4; ++j) { const int c = j * 256 + lane * 4; st_bf4(xb + (size_t)t * DM + c, v[i][j]); }
;                 if (lane < 16) part[(size_t)t * 16 + lane] = lane == 0 ? s : 0.f;
.LBB0_1653:
	s_waitcnt vmcnt(11)
	v_lshlrev_b32_e32 v16, 16, v32
	v_and_b32_e32 v17, 0xffff0000, v32
	v_lshlrev_b32_e32 v20, 16, v33
	v_and_b32_e32 v21, 0xffff0000, v33
	s_waitcnt vmcnt(10)
	v_lshlrev_b32_e32 v32, 16, v30
	v_and_b32_e32 v33, 0xffff0000, v30
	v_lshlrev_b32_e32 v30, 16, v31
	v_and_b32_e32 v31, 0xffff0000, v31
	s_waitcnt vmcnt(9)
	v_lshlrev_b32_e32 v48, 16, v34
	v_and_b32_e32 v49, 0xffff0000, v34
	v_lshlrev_b32_e32 v34, 16, v35
	v_and_b32_e32 v35, 0xffff0000, v35
	v_pk_fma_f32 v[16:17], v[150:151], v[32:33], v[16:17] op_sel_hi:[0,1,1]
	v_pk_fma_f32 v[20:21], v[150:151], v[30:31], v[20:21] op_sel_hi:[0,1,1]
	v_pk_fma_f32 v[30:31], v[150:151], v[34:35], v[20:21] op_sel:[1,0,0]
	v_pk_fma_f32 v[32:33], v[150:151], v[48:49], v[16:17] op_sel:[1,0,0]
	v_mul_f32_e32 v17, v31, v31
	v_mul_f32_e32 v16, v33, v33
	v_fmac_f32_e32 v16, v32, v32
	v_fmac_f32_e32 v17, v30, v30
	s_waitcnt vmcnt(8)
	v_lshlrev_b32_e32 v36, 16, v40
	v_and_b32_e32 v37, 0xffff0000, v40
	v_lshlrev_b32_e32 v38, 16, v41
	v_and_b32_e32 v39, 0xffff0000, v41
	v_add_f32_e32 v48, v16, v17
	s_waitcnt vmcnt(7)
	v_lshlrev_b32_e32 v16, 16, v26
	v_and_b32_e32 v17, 0xffff0000, v26
	v_lshlrev_b32_e32 v20, 16, v27
	v_and_b32_e32 v21, 0xffff0000, v27
	s_waitcnt vmcnt(6)
	v_lshlrev_b32_e32 v26, 16, v28
	v_and_b32_e32 v27, 0xffff0000, v28
	v_lshlrev_b32_e32 v28, 16, v29
	v_and_b32_e32 v29, 0xffff0000, v29
	v_pk_fma_f32 v[34:35], v[150:151], v[16:17], v[36:37] op_sel_hi:[0,1,1]
	v_pk_fma_f32 v[16:17], v[150:151], v[20:21], v[38:39] op_sel_hi:[0,1,1]
	v_pk_fma_f32 v[16:17], v[150:151], v[28:29], v[16:17] op_sel:[1,0,0]
	v_pk_fma_f32 v[26:27], v[150:151], v[26:27], v[34:35] op_sel:[1,0,0]
	v_mul_f32_e32 v21, v17, v17
	v_mul_f32_e32 v20, v27, v27
	v_fmac_f32_e32 v20, v26, v26
	v_fmac_f32_e32 v21, v16, v16
	v_add_f32_e32 v20, v20, v21
	s_waitcnt vmcnt(5)
	v_lshlrev_b32_e32 v40, 16, v42
	v_and_b32_e32 v41, 0xffff0000, v42
	v_lshlrev_b32_e32 v42, 16, v43
	v_and_b32_e32 v43, 0xffff0000, v43
	v_add_f32_e32 v36, v48, v20
	s_waitcnt vmcnt(4)
	v_lshlrev_b32_e32 v20, 16, v22
	v_and_b32_e32 v21, 0xffff0000, v22
	v_lshlrev_b32_e32 v22, 16, v23
	v_and_b32_e32 v23, 0xffff0000, v23
	s_waitcnt vmcnt(3)
	v_lshlrev_b32_e32 v28, 16, v24
	v_and_b32_e32 v29, 0xffff0000, v24
	v_lshlrev_b32_e32 v24, 16, v25
	v_and_b32_e32 v25, 0xffff0000, v25
	v_pk_fma_f32 v[34:35], v[150:151], v[20:21], v[40:41] op_sel_hi:[0,1,1]
	v_pk_fma_f32 v[20:21], v[150:151], v[22:23], v[42:43] op_sel_hi:[0,1,1]
	v_pk_fma_f32 v[20:21], v[150:151], v[24:25], v[20:21] op_sel:[1,0,0]
	v_pk_fma_f32 v[24:25], v[150:151], v[28:29], v[34:35] op_sel:[1,0,0]
	v_mul_f32_e32 v23, v21, v21
	v_mul_f32_e32 v22, v25, v25
	v_fmac_f32_e32 v22, v24, v24
	v_fmac_f32_e32 v23, v20, v20
	v_add_f32_e32 v22, v22, v23
	s_waitcnt vmcnt(2)
	v_lshlrev_b32_e32 v44, 16, v70
	v_and_b32_e32 v45, 0xffff0000, v70
	v_lshlrev_b32_e32 v46, 16, v71
	v_and_b32_e32 v47, 0xffff0000, v71
	v_add_f32_e32 v40, v36, v22
	s_waitcnt vmcnt(1)
	v_lshlrev_b32_e32 v22, 16, v66
	v_and_b32_e32 v23, 0xffff0000, v66
	v_lshlrev_b32_e32 v28, 16, v67
	v_and_b32_e32 v29, 0xffff0000, v67
	s_waitcnt vmcnt(0)
	v_lshlrev_b32_e32 v34, 16, v68
	v_and_b32_e32 v35, 0xffff0000, v68
	v_lshlrev_b32_e32 v36, 16, v69
	v_and_b32_e32 v37, 0xffff0000, v69
	v_pk_fma_f32 v[38:39], v[150:151], v[22:23], v[44:45] op_sel_hi:[0,1,1]
	v_pk_fma_f32 v[22:23], v[150:151], v[28:29], v[46:47] op_sel_hi:[0,1,1]
	v_pk_fma_f32 v[22:23], v[150:151], v[36:37], v[22:23] op_sel:[1,0,0]
	v_pk_fma_f32 v[14:15], v[150:151], v[34:35], v[38:39] op_sel:[1,0,0]
	v_mul_f32_e32 v29, v23, v23
	v_mul_f32_e32 v28, v15, v15
	v_fmac_f32_e32 v28, v14, v14
	v_fmac_f32_e32 v29, v22, v22
	v_add_f32_e32 v28, v28, v29
	v_add_f32_e32 v28, v40, v28
	ds_swizzle_b32 v29, v28 offset:swizzle(SWAP,1)
	s_andn2_b64 vcc, exec, s[20:21]
	s_waitcnt lgkmcnt(0)
	v_add_f32_e32 v28, v28, v29
	ds_swizzle_b32 v29, v28 offset:swizzle(SWAP,2)
	s_waitcnt lgkmcnt(0)
	v_add_f32_e32 v28, v28, v29
	ds_swizzle_b32 v29, v28 offset:swizzle(SWAP,4)
	s_waitcnt lgkmcnt(0)
	v_add_f32_e32 v28, v28, v29
	ds_swizzle_b32 v29, v28 offset:swizzle(SWAP,8)
	s_waitcnt lgkmcnt(0)
	v_add_f32_e32 v28, v28, v29
	ds_swizzle_b32 v29, v28 offset:swizzle(SWAP,16)
	s_waitcnt lgkmcnt(0)
	v_add_f32_e32 v28, v28, v29
	v_mov_b32_e32 v29, v28
	s_nop 1
	v_permlane32_swap_b32_e32 v28, v29
	s_cbranch_vccnz .LBB0_1632
	v_add_f32_e32 v28, v28, v29
	s_and_b64 vcc, exec, s[6:7]
	s_mov_b64 s[6:7], -1
	s_cbranch_vccnz .LBB0_1658
	v_cvt_pk_bf16_f32 v34, v32, v33
	v_cvt_pk_bf16_f32 v35, v30, v31
	global_store_dwordx2 v[18:19], v[34:35], off
	v_cvt_pk_bf16_f32 v34, v26, v27
	v_cvt_pk_bf16_f32 v35, v16, v17
	global_store_dwordx2 v[18:19], v[34:35], off offset:512
	v_cvt_pk_bf16_f32 v34, v24, v25
	v_cvt_pk_bf16_f32 v35, v20, v21
	global_store_dwordx2 v[18:19], v[34:35], off offset:1024
	v_cvt_pk_bf16_f32 v34, v14, v15
	v_cvt_pk_bf16_f32 v35, v22, v23
	global_store_dwordx2 v[18:19], v[34:35], off offset:1536
	s_and_saveexec_b64 s[6:7], s[0:1]
	s_cbranch_execz .LBB0_1657
	s_lshl_b64 s[2:3], s[18:19], 6
	v_cndmask_b32_e64 v29, 0, v28, s[4:5]
	v_lshl_add_u64 v[18:19], v[0:1], 0, s[2:3]
	global_store_dword v[18:19], v29, off
